# GEMM load phases (P2/P4/P7): LDS-DMA requests issued ahead of the fragment ds_reads inside the same barrier interval
# speedup vs baseline: 1.0121x; 1.0121x over previous
.LBB0_183:
	s_add_i32 s70, s70, 2
	s_waitcnt vmcnt(8)
	s_add_u32 s48, s44, 0x80
	s_waitcnt lgkmcnt(0)
	s_addc_u32 s49, s45, 0
	s_and_b64 s[46:47], s[46:47], exec
	v_mov_b32_e32 v201, v199
	v_mov_b32_e32 v205, v199
	s_cselect_b32 s47, s80, s49
	s_cselect_b32 s46, s81, s48
	s_cselect_b32 s49, s82, s69
	s_cselect_b32 s48, s83, s68
	s_barrier
	s_setprio 1
	s_waitcnt lgkmcnt(0)
	v_mfma_scale_f32_16x16x128_f8f6f4 v[190:193], v[18:25], v[58:65], v[190:193], v215, v215 op_sel_hi:[0,0,0]
	v_mfma_scale_f32_16x16x128_f8f6f4 v[186:189], v[26:33], v[58:65], v[186:189], v215, v215 op_sel_hi:[0,0,0]
	v_mfma_scale_f32_16x16x128_f8f6f4 v[174:177], v[18:25], v[50:57], v[174:177], v215, v215 op_sel_hi:[0,0,0]
	v_mfma_scale_f32_16x16x128_f8f6f4 v[170:173], v[26:33], v[50:57], v[170:173], v215, v215 op_sel_hi:[0,0,0]
	v_mfma_scale_f32_16x16x128_f8f6f4 v[158:161], v[18:25], v[42:49], v[158:161], v215, v215 op_sel_hi:[0,0,0]
	v_mfma_scale_f32_16x16x128_f8f6f4 v[154:157], v[26:33], v[42:49], v[154:157], v215, v215 op_sel_hi:[0,0,0]
	v_mfma_scale_f32_16x16x128_f8f6f4 v[142:145], v[18:25], v[34:41], v[142:145], v215, v215 op_sel_hi:[0,0,0]
	v_mfma_scale_f32_16x16x128_f8f6f4 v[138:141], v[26:33], v[34:41], v[138:141], v215, v215 op_sel_hi:[0,0,0]
	s_setprio 0
	s_setprio 1
	v_mfma_scale_f32_16x16x128_f8f6f4 v[182:185], v[2:9], v[58:65], v[182:185], v215, v215 op_sel_hi:[0,0,0]
	v_mfma_scale_f32_16x16x128_f8f6f4 v[178:181], v[10:17], v[58:65], v[178:181], v215, v215 op_sel_hi:[0,0,0]
	v_mfma_scale_f32_16x16x128_f8f6f4 v[166:169], v[2:9], v[50:57], v[166:169], v215, v215 op_sel_hi:[0,0,0]
	v_mfma_scale_f32_16x16x128_f8f6f4 v[162:165], v[10:17], v[50:57], v[162:165], v215, v215 op_sel_hi:[0,0,0]
	v_mfma_scale_f32_16x16x128_f8f6f4 v[150:153], v[2:9], v[42:49], v[150:153], v215, v215 op_sel_hi:[0,0,0]
	v_mfma_scale_f32_16x16x128_f8f6f4 v[146:149], v[10:17], v[42:49], v[146:149], v215, v215 op_sel_hi:[0,0,0]
	v_mfma_scale_f32_16x16x128_f8f6f4 v[134:137], v[2:9], v[34:41], v[134:137], v215, v215 op_sel_hi:[0,0,0]
	v_mfma_scale_f32_16x16x128_f8f6f4 v[130:133], v[10:17], v[34:41], v[130:133], v215, v215 op_sel_hi:[0,0,0]
	s_setprio 0
	s_barrier
	s_mov_b32 m0, s56
	v_lshl_add_u64 v[218:219], s[48:49], 0, v[194:195]
	v_lshl_add_u64 v[220:221], s[48:49], 0, v[196:197]
	s_add_u32 s48, s48, s18
	global_load_lds_dwordx4 v[218:219], off
	s_mov_b32 m0, s57
	s_addc_u32 s49, s49, s19
	global_load_lds_dwordx4 v[220:221], off
	v_lshl_add_u64 v[222:223], s[48:49], 0, v[194:195]
	s_mov_b32 m0, s58
	v_lshl_add_u64 v[224:225], s[48:49], 0, v[196:197]
	global_load_lds_dwordx4 v[222:223], off
	s_mov_b32 m0, s59
	v_mov_b32_e32 v203, v199
	global_load_lds_dwordx4 v[224:225], off
	s_mov_b32 m0, s55
	v_lshl_add_u64 v[226:227], s[46:47], 0, v[198:199]
	global_load_lds_dwordx4 v198, s[46:47]
	s_mov_b32 m0, s60
	v_lshl_add_u64 v[228:229], s[46:47], 0, v[202:203]
	global_load_lds_dwordx4 v202, s[46:47]
	ds_read_b128 v[34:37], v214 offset:16384
	ds_read_b128 v[38:41], v214 offset:17408
	ds_read_b128 v[42:45], v214 offset:18432
	ds_read_b128 v[46:49], v214 offset:19456
	ds_read_b128 v[50:53], v214 offset:20480
	ds_read_b128 v[54:57], v214 offset:21504
	ds_read_b128 v[58:61], v214 offset:22528
	ds_read_b128 v[62:65], v214 offset:23552
	s_waitcnt vmcnt(8)
	s_waitcnt lgkmcnt(0)
	s_barrier
	s_setprio 1
	s_waitcnt lgkmcnt(0)
	v_mfma_scale_f32_16x16x128_f8f6f4 v[126:129], v[18:25], v[34:41], v[126:129], v215, v215 op_sel_hi:[0,0,0]
	v_mfma_scale_f32_16x16x128_f8f6f4 v[122:125], v[26:33], v[34:41], v[122:125], v215, v215 op_sel_hi:[0,0,0]
	v_mfma_scale_f32_16x16x128_f8f6f4 v[110:113], v[18:25], v[42:49], v[110:113], v215, v215 op_sel_hi:[0,0,0]
	v_mfma_scale_f32_16x16x128_f8f6f4 v[106:109], v[26:33], v[42:49], v[106:109], v215, v215 op_sel_hi:[0,0,0]
	v_mfma_scale_f32_16x16x128_f8f6f4 v[94:97], v[18:25], v[50:57], v[94:97], v215, v215 op_sel_hi:[0,0,0]
	v_mfma_scale_f32_16x16x128_f8f6f4 v[90:93], v[26:33], v[50:57], v[90:93], v215, v215 op_sel_hi:[0,0,0]
	v_mfma_scale_f32_16x16x128_f8f6f4 v[78:81], v[18:25], v[58:65], v[78:81], v215, v215 op_sel_hi:[0,0,0]
	v_mfma_scale_f32_16x16x128_f8f6f4 v[74:77], v[26:33], v[58:65], v[74:77], v215, v215 op_sel_hi:[0,0,0]
	s_setprio 0
	s_setprio 1
	v_mfma_scale_f32_16x16x128_f8f6f4 v[118:121], v[2:9], v[34:41], v[118:121], v215, v215 op_sel_hi:[0,0,0]
	v_mfma_scale_f32_16x16x128_f8f6f4 v[114:117], v[10:17], v[34:41], v[114:117], v215, v215 op_sel_hi:[0,0,0]
	v_mfma_scale_f32_16x16x128_f8f6f4 v[102:105], v[2:9], v[42:49], v[102:105], v215, v215 op_sel_hi:[0,0,0]
	v_mfma_scale_f32_16x16x128_f8f6f4 v[98:101], v[10:17], v[42:49], v[98:101], v215, v215 op_sel_hi:[0,0,0]
	v_mfma_scale_f32_16x16x128_f8f6f4 v[86:89], v[2:9], v[50:57], v[86:89], v215, v215 op_sel_hi:[0,0,0]
	v_mfma_scale_f32_16x16x128_f8f6f4 v[82:85], v[10:17], v[50:57], v[82:85], v215, v215 op_sel_hi:[0,0,0]
	v_mfma_scale_f32_16x16x128_f8f6f4 v[70:73], v[2:9], v[58:65], v[70:73], v215, v215 op_sel_hi:[0,0,0]
	v_mfma_scale_f32_16x16x128_f8f6f4 v[66:69], v[10:17], v[58:65], v[66:69], v215, v215 op_sel_hi:[0,0,0]
	s_setprio 0
	s_barrier
	s_add_i32 s48, 0, 0x18000
	s_add_i32 s49, 0, 0x1c000
	v_add_u32_e32 v14, s48, v210
	v_add_u32_e32 v30, s49, v210
	s_mov_b32 m0, s61
	v_lshl_add_u64 v[230:231], s[46:47], 0, v[200:201]
	global_load_lds_dwordx4 v[230:231], off
	v_lshl_add_u64 v[230:231], s[46:47], 0, v[204:205]
	s_mov_b32 m0, s62
	s_nop 0
	global_load_lds_dwordx4 v[230:231], off
	ds_read_b128 v[2:5], v14
	ds_read_b128 v[6:9], v14 offset:1024
	ds_read_b128 v[10:13], v14 offset:2048
	ds_read_b128 v[14:17], v14 offset:3072
	ds_read_b128 v[18:21], v30
	ds_read_b128 v[22:25], v30 offset:1024
	ds_read_b128 v[26:29], v30 offset:2048
	ds_read_b128 v[30:33], v30 offset:3072
	ds_read_b128 v[34:37], v214 offset:32768
	ds_read_b128 v[38:41], v214 offset:33792
	ds_read_b128 v[42:45], v214 offset:34816
	ds_read_b128 v[46:49], v214 offset:35840
	ds_read_b128 v[50:53], v214 offset:36864
	ds_read_b128 v[54:57], v214 offset:37888
	ds_read_b128 v[58:61], v214 offset:38912
	ds_read_b128 v[62:65], v214 offset:39936
	s_waitcnt vmcnt(8)
	s_waitcnt lgkmcnt(0)
	s_barrier
	s_setprio 1
	s_waitcnt lgkmcnt(0)
	v_mfma_scale_f32_16x16x128_f8f6f4 v[190:193], v[2:9], v[34:41], v[190:193], v215, v215 op_sel_hi:[0,0,0]
	v_mfma_scale_f32_16x16x128_f8f6f4 v[186:189], v[10:17], v[34:41], v[186:189], v215, v215 op_sel_hi:[0,0,0]
	v_mfma_scale_f32_16x16x128_f8f6f4 v[174:177], v[2:9], v[42:49], v[174:177], v215, v215 op_sel_hi:[0,0,0]
	v_mfma_scale_f32_16x16x128_f8f6f4 v[170:173], v[10:17], v[42:49], v[170:173], v215, v215 op_sel_hi:[0,0,0]
	v_mfma_scale_f32_16x16x128_f8f6f4 v[158:161], v[2:9], v[50:57], v[158:161], v215, v215 op_sel_hi:[0,0,0]
	v_mfma_scale_f32_16x16x128_f8f6f4 v[154:157], v[10:17], v[50:57], v[154:157], v215, v215 op_sel_hi:[0,0,0]
	v_mfma_scale_f32_16x16x128_f8f6f4 v[142:145], v[2:9], v[58:65], v[142:145], v215, v215 op_sel_hi:[0,0,0]
	v_mfma_scale_f32_16x16x128_f8f6f4 v[138:141], v[10:17], v[58:65], v[138:141], v215, v215 op_sel_hi:[0,0,0]
	s_setprio 0
	s_setprio 1
	v_mfma_scale_f32_16x16x128_f8f6f4 v[182:185], v[18:25], v[34:41], v[182:185], v215, v215 op_sel_hi:[0,0,0]
	v_mfma_scale_f32_16x16x128_f8f6f4 v[178:181], v[26:33], v[34:41], v[178:181], v215, v215 op_sel_hi:[0,0,0]
	v_mfma_scale_f32_16x16x128_f8f6f4 v[166:169], v[18:25], v[42:49], v[166:169], v215, v215 op_sel_hi:[0,0,0]
	v_mfma_scale_f32_16x16x128_f8f6f4 v[162:165], v[26:33], v[42:49], v[162:165], v215, v215 op_sel_hi:[0,0,0]
	v_mfma_scale_f32_16x16x128_f8f6f4 v[150:153], v[18:25], v[50:57], v[150:153], v215, v215 op_sel_hi:[0,0,0]
	v_mfma_scale_f32_16x16x128_f8f6f4 v[146:149], v[26:33], v[50:57], v[146:149], v215, v215 op_sel_hi:[0,0,0]
	v_mfma_scale_f32_16x16x128_f8f6f4 v[134:137], v[18:25], v[58:65], v[134:137], v215, v215 op_sel_hi:[0,0,0]
	v_mfma_scale_f32_16x16x128_f8f6f4 v[130:133], v[26:33], v[58:65], v[130:133], v215, v215 op_sel_hi:[0,0,0]
	s_setprio 0
	s_barrier
	s_add_i32 s46, s48, s53
	v_lshl_add_u64 v[218:219], v[218:219], 0, s[22:23]
	s_mov_b32 m0, s46
	s_nop 0
	global_load_lds_dwordx4 v[218:219], off
	v_lshl_add_u64 v[218:219], v[220:221], 0, s[22:23]
	s_add_i32 m0, s46, 0x2000
	s_add_i32 s46, s49, s53
	global_load_lds_dwordx4 v[218:219], off
	v_lshl_add_u64 v[218:219], v[222:223], 0, s[22:23]
	s_mov_b32 m0, s46
	s_nop 0
	global_load_lds_dwordx4 v[218:219], off
	v_lshl_add_u64 v[218:219], v[224:225], 0, s[22:23]
	s_add_i32 m0, s46, 0x2000
	s_nop 0
	global_load_lds_dwordx4 v[218:219], off
	v_lshl_add_u64 v[218:219], v[226:227], 0, s[22:23]
	s_mov_b32 m0, s65
	s_nop 0
	global_load_lds_dwordx4 v[218:219], off
	v_lshl_add_u64 v[218:219], v[228:229], 0, s[22:23]
	s_mov_b32 m0, s66
	s_nop 0
	global_load_lds_dwordx4 v[218:219], off
	ds_read_b128 v[34:37], v214 offset:49152
	ds_read_b128 v[38:41], v214 offset:50176
	ds_read_b128 v[42:45], v214 offset:51200
	ds_read_b128 v[46:49], v214 offset:52224
	ds_read_b128 v[50:53], v214 offset:53248
	ds_read_b128 v[54:57], v214 offset:54272
	ds_read_b128 v[58:61], v214 offset:55296
	ds_read_b128 v[62:65], v214 offset:56320
	s_waitcnt vmcnt(8)
	s_waitcnt lgkmcnt(0)
	s_barrier
	s_setprio 1
	s_waitcnt lgkmcnt(0)
	v_mfma_scale_f32_16x16x128_f8f6f4 v[126:129], v[2:9], v[34:41], v[126:129], v215, v215 op_sel_hi:[0,0,0]
	v_mfma_scale_f32_16x16x128_f8f6f4 v[122:125], v[10:17], v[34:41], v[122:125], v215, v215 op_sel_hi:[0,0,0]
	v_mfma_scale_f32_16x16x128_f8f6f4 v[110:113], v[2:9], v[42:49], v[110:113], v215, v215 op_sel_hi:[0,0,0]
	v_mfma_scale_f32_16x16x128_f8f6f4 v[106:109], v[10:17], v[42:49], v[106:109], v215, v215 op_sel_hi:[0,0,0]
	v_mfma_scale_f32_16x16x128_f8f6f4 v[94:97], v[2:9], v[50:57], v[94:97], v215, v215 op_sel_hi:[0,0,0]
	v_mfma_scale_f32_16x16x128_f8f6f4 v[90:93], v[10:17], v[50:57], v[90:93], v215, v215 op_sel_hi:[0,0,0]
	v_mfma_scale_f32_16x16x128_f8f6f4 v[78:81], v[2:9], v[58:65], v[78:81], v215, v215 op_sel_hi:[0,0,0]
	v_mfma_scale_f32_16x16x128_f8f6f4 v[74:77], v[10:17], v[58:65], v[74:77], v215, v215 op_sel_hi:[0,0,0]
	s_setprio 0
	s_setprio 1
	v_mfma_scale_f32_16x16x128_f8f6f4 v[118:121], v[18:25], v[34:41], v[118:121], v215, v215 op_sel_hi:[0,0,0]
	v_mfma_scale_f32_16x16x128_f8f6f4 v[114:117], v[26:33], v[34:41], v[114:117], v215, v215 op_sel_hi:[0,0,0]
	v_mfma_scale_f32_16x16x128_f8f6f4 v[102:105], v[18:25], v[42:49], v[102:105], v215, v215 op_sel_hi:[0,0,0]
	v_mfma_scale_f32_16x16x128_f8f6f4 v[98:101], v[26:33], v[42:49], v[98:101], v215, v215 op_sel_hi:[0,0,0]
	v_mfma_scale_f32_16x16x128_f8f6f4 v[86:89], v[18:25], v[50:57], v[86:89], v215, v215 op_sel_hi:[0,0,0]
	v_mfma_scale_f32_16x16x128_f8f6f4 v[82:85], v[26:33], v[50:57], v[82:85], v215, v215 op_sel_hi:[0,0,0]
	v_mfma_scale_f32_16x16x128_f8f6f4 v[70:73], v[18:25], v[58:65], v[70:73], v215, v215 op_sel_hi:[0,0,0]
	v_mfma_scale_f32_16x16x128_f8f6f4 v[66:69], v[26:33], v[58:65], v[66:69], v215, v215 op_sel_hi:[0,0,0]
	s_setprio 0
	s_barrier
	s_add_u32 s44, s44, 0x100
	s_addc_u32 s45, s45, 0
	s_add_u32 s68, s68, 0x100
	s_addc_u32 s69, s69, 0
	s_cmp_ge_i32 s70, s15
	s_cbranch_scc1 .LBB0_187

.LBB0_233:
	s_add_i32 s70, s70, 2
	s_waitcnt vmcnt(8)
	s_add_u32 s44, s40, 0x80
	s_waitcnt lgkmcnt(0)
	s_addc_u32 s45, s41, 0
	s_and_b64 s[42:43], s[42:43], exec
	v_mov_b32_e32 v201, v199
	v_mov_b32_e32 v205, v199
	s_cselect_b32 s43, s73, s45
	s_cselect_b32 s42, s74, s44
	s_cselect_b32 s45, s75, s69
	s_cselect_b32 s44, s76, s68
	s_barrier
	s_setprio 1
	s_waitcnt lgkmcnt(0)
	v_mfma_scale_f32_16x16x128_f8f6f4 v[190:193], v[18:25], v[58:65], v[190:193], v214, v214 op_sel_hi:[0,0,0]
	v_mfma_scale_f32_16x16x128_f8f6f4 v[186:189], v[26:33], v[58:65], v[186:189], v214, v214 op_sel_hi:[0,0,0]
	v_mfma_scale_f32_16x16x128_f8f6f4 v[174:177], v[18:25], v[50:57], v[174:177], v214, v214 op_sel_hi:[0,0,0]
	v_mfma_scale_f32_16x16x128_f8f6f4 v[170:173], v[26:33], v[50:57], v[170:173], v214, v214 op_sel_hi:[0,0,0]
	v_mfma_scale_f32_16x16x128_f8f6f4 v[158:161], v[18:25], v[42:49], v[158:161], v214, v214 op_sel_hi:[0,0,0]
	v_mfma_scale_f32_16x16x128_f8f6f4 v[154:157], v[26:33], v[42:49], v[154:157], v214, v214 op_sel_hi:[0,0,0]
	v_mfma_scale_f32_16x16x128_f8f6f4 v[142:145], v[18:25], v[34:41], v[142:145], v214, v214 op_sel_hi:[0,0,0]
	v_mfma_scale_f32_16x16x128_f8f6f4 v[138:141], v[26:33], v[34:41], v[138:141], v214, v214 op_sel_hi:[0,0,0]
	s_setprio 0
	s_setprio 1
	v_mfma_scale_f32_16x16x128_f8f6f4 v[182:185], v[2:9], v[58:65], v[182:185], v214, v214 op_sel_hi:[0,0,0]
	v_mfma_scale_f32_16x16x128_f8f6f4 v[178:181], v[10:17], v[58:65], v[178:181], v214, v214 op_sel_hi:[0,0,0]
	v_mfma_scale_f32_16x16x128_f8f6f4 v[166:169], v[2:9], v[50:57], v[166:169], v214, v214 op_sel_hi:[0,0,0]
	v_mfma_scale_f32_16x16x128_f8f6f4 v[162:165], v[10:17], v[50:57], v[162:165], v214, v214 op_sel_hi:[0,0,0]
	v_mfma_scale_f32_16x16x128_f8f6f4 v[150:153], v[2:9], v[42:49], v[150:153], v214, v214 op_sel_hi:[0,0,0]
	v_mfma_scale_f32_16x16x128_f8f6f4 v[146:149], v[10:17], v[42:49], v[146:149], v214, v214 op_sel_hi:[0,0,0]
	v_mfma_scale_f32_16x16x128_f8f6f4 v[134:137], v[2:9], v[34:41], v[134:137], v214, v214 op_sel_hi:[0,0,0]
	v_mfma_scale_f32_16x16x128_f8f6f4 v[130:133], v[10:17], v[34:41], v[130:133], v214, v214 op_sel_hi:[0,0,0]
	s_setprio 0
	s_barrier
	s_mov_b32 m0, s51
	v_lshl_add_u64 v[218:219], s[44:45], 0, v[194:195]
	v_lshl_add_u64 v[220:221], s[44:45], 0, v[196:197]
	s_add_u32 s44, s44, s12
	global_load_lds_dwordx4 v[218:219], off
	s_mov_b32 m0, s52
	s_addc_u32 s45, s45, s13
	global_load_lds_dwordx4 v[220:221], off
	v_lshl_add_u64 v[222:223], s[44:45], 0, v[194:195]
	s_mov_b32 m0, s53
	v_lshl_add_u64 v[224:225], s[44:45], 0, v[196:197]
	global_load_lds_dwordx4 v[222:223], off
	s_mov_b32 m0, s54
	v_mov_b32_e32 v203, v199
	global_load_lds_dwordx4 v[224:225], off
	s_mov_b32 m0, s49
	v_lshl_add_u64 v[226:227], s[42:43], 0, v[198:199]
	global_load_lds_dwordx4 v198, s[42:43]
	s_mov_b32 m0, s55
	v_lshl_add_u64 v[228:229], s[42:43], 0, v[202:203]
	global_load_lds_dwordx4 v202, s[42:43]
	ds_read_b128 v[34:37], v213 offset:16384
	ds_read_b128 v[38:41], v213 offset:17408
	ds_read_b128 v[42:45], v213 offset:18432
	ds_read_b128 v[46:49], v213 offset:19456
	ds_read_b128 v[50:53], v213 offset:20480
	ds_read_b128 v[54:57], v213 offset:21504
	ds_read_b128 v[58:61], v213 offset:22528
	ds_read_b128 v[62:65], v213 offset:23552
	s_waitcnt vmcnt(8)
	s_waitcnt lgkmcnt(0)
	s_barrier
	s_setprio 1
	s_waitcnt lgkmcnt(0)
	v_mfma_scale_f32_16x16x128_f8f6f4 v[126:129], v[18:25], v[34:41], v[126:129], v214, v214 op_sel_hi:[0,0,0]
	v_mfma_scale_f32_16x16x128_f8f6f4 v[122:125], v[26:33], v[34:41], v[122:125], v214, v214 op_sel_hi:[0,0,0]
	v_mfma_scale_f32_16x16x128_f8f6f4 v[110:113], v[18:25], v[42:49], v[110:113], v214, v214 op_sel_hi:[0,0,0]
	v_mfma_scale_f32_16x16x128_f8f6f4 v[106:109], v[26:33], v[42:49], v[106:109], v214, v214 op_sel_hi:[0,0,0]
	v_mfma_scale_f32_16x16x128_f8f6f4 v[94:97], v[18:25], v[50:57], v[94:97], v214, v214 op_sel_hi:[0,0,0]
	v_mfma_scale_f32_16x16x128_f8f6f4 v[90:93], v[26:33], v[50:57], v[90:93], v214, v214 op_sel_hi:[0,0,0]
	v_mfma_scale_f32_16x16x128_f8f6f4 v[78:81], v[18:25], v[58:65], v[78:81], v214, v214 op_sel_hi:[0,0,0]
	v_mfma_scale_f32_16x16x128_f8f6f4 v[74:77], v[26:33], v[58:65], v[74:77], v214, v214 op_sel_hi:[0,0,0]
	s_setprio 0
	s_setprio 1
	v_mfma_scale_f32_16x16x128_f8f6f4 v[118:121], v[2:9], v[34:41], v[118:121], v214, v214 op_sel_hi:[0,0,0]
	v_mfma_scale_f32_16x16x128_f8f6f4 v[114:117], v[10:17], v[34:41], v[114:117], v214, v214 op_sel_hi:[0,0,0]
	v_mfma_scale_f32_16x16x128_f8f6f4 v[102:105], v[2:9], v[42:49], v[102:105], v214, v214 op_sel_hi:[0,0,0]
	v_mfma_scale_f32_16x16x128_f8f6f4 v[98:101], v[10:17], v[42:49], v[98:101], v214, v214 op_sel_hi:[0,0,0]
	v_mfma_scale_f32_16x16x128_f8f6f4 v[86:89], v[2:9], v[50:57], v[86:89], v214, v214 op_sel_hi:[0,0,0]
	v_mfma_scale_f32_16x16x128_f8f6f4 v[82:85], v[10:17], v[50:57], v[82:85], v214, v214 op_sel_hi:[0,0,0]
	v_mfma_scale_f32_16x16x128_f8f6f4 v[70:73], v[2:9], v[58:65], v[70:73], v214, v214 op_sel_hi:[0,0,0]
	v_mfma_scale_f32_16x16x128_f8f6f4 v[66:69], v[10:17], v[58:65], v[66:69], v214, v214 op_sel_hi:[0,0,0]
	s_setprio 0
	s_barrier
	s_add_i32 s44, 0, 0x18000
	s_add_i32 s45, 0, 0x1c000
	v_add_u32_e32 v14, s44, v209
	v_add_u32_e32 v30, s45, v209
	s_mov_b32 m0, s56
	v_lshl_add_u64 v[230:231], s[42:43], 0, v[200:201]
	global_load_lds_dwordx4 v[230:231], off
	v_lshl_add_u64 v[230:231], s[42:43], 0, v[204:205]
	s_mov_b32 m0, s57
	s_nop 0
	global_load_lds_dwordx4 v[230:231], off
	ds_read_b128 v[2:5], v14
	ds_read_b128 v[6:9], v14 offset:1024
	ds_read_b128 v[10:13], v14 offset:2048
	ds_read_b128 v[14:17], v14 offset:3072
	ds_read_b128 v[18:21], v30
	ds_read_b128 v[22:25], v30 offset:1024
	ds_read_b128 v[26:29], v30 offset:2048
	ds_read_b128 v[30:33], v30 offset:3072
	ds_read_b128 v[34:37], v213 offset:32768
	ds_read_b128 v[38:41], v213 offset:33792
	ds_read_b128 v[42:45], v213 offset:34816
	ds_read_b128 v[46:49], v213 offset:35840
	ds_read_b128 v[50:53], v213 offset:36864
	ds_read_b128 v[54:57], v213 offset:37888
	ds_read_b128 v[58:61], v213 offset:38912
	ds_read_b128 v[62:65], v213 offset:39936
	s_waitcnt vmcnt(8)
	s_waitcnt lgkmcnt(0)
	s_barrier
	s_setprio 1
	s_waitcnt lgkmcnt(0)
	v_mfma_scale_f32_16x16x128_f8f6f4 v[190:193], v[2:9], v[34:41], v[190:193], v214, v214 op_sel_hi:[0,0,0]
	v_mfma_scale_f32_16x16x128_f8f6f4 v[186:189], v[10:17], v[34:41], v[186:189], v214, v214 op_sel_hi:[0,0,0]
	v_mfma_scale_f32_16x16x128_f8f6f4 v[174:177], v[2:9], v[42:49], v[174:177], v214, v214 op_sel_hi:[0,0,0]
	v_mfma_scale_f32_16x16x128_f8f6f4 v[170:173], v[10:17], v[42:49], v[170:173], v214, v214 op_sel_hi:[0,0,0]
	v_mfma_scale_f32_16x16x128_f8f6f4 v[158:161], v[2:9], v[50:57], v[158:161], v214, v214 op_sel_hi:[0,0,0]
	v_mfma_scale_f32_16x16x128_f8f6f4 v[154:157], v[10:17], v[50:57], v[154:157], v214, v214 op_sel_hi:[0,0,0]
	v_mfma_scale_f32_16x16x128_f8f6f4 v[142:145], v[2:9], v[58:65], v[142:145], v214, v214 op_sel_hi:[0,0,0]
	v_mfma_scale_f32_16x16x128_f8f6f4 v[138:141], v[10:17], v[58:65], v[138:141], v214, v214 op_sel_hi:[0,0,0]
	s_setprio 0
	s_setprio 1
	v_mfma_scale_f32_16x16x128_f8f6f4 v[182:185], v[18:25], v[34:41], v[182:185], v214, v214 op_sel_hi:[0,0,0]
	v_mfma_scale_f32_16x16x128_f8f6f4 v[178:181], v[26:33], v[34:41], v[178:181], v214, v214 op_sel_hi:[0,0,0]
	v_mfma_scale_f32_16x16x128_f8f6f4 v[166:169], v[18:25], v[42:49], v[166:169], v214, v214 op_sel_hi:[0,0,0]
	v_mfma_scale_f32_16x16x128_f8f6f4 v[162:165], v[26:33], v[42:49], v[162:165], v214, v214 op_sel_hi:[0,0,0]
	v_mfma_scale_f32_16x16x128_f8f6f4 v[150:153], v[18:25], v[50:57], v[150:153], v214, v214 op_sel_hi:[0,0,0]
	v_mfma_scale_f32_16x16x128_f8f6f4 v[146:149], v[26:33], v[50:57], v[146:149], v214, v214 op_sel_hi:[0,0,0]
	v_mfma_scale_f32_16x16x128_f8f6f4 v[134:137], v[18:25], v[58:65], v[134:137], v214, v214 op_sel_hi:[0,0,0]
	v_mfma_scale_f32_16x16x128_f8f6f4 v[130:133], v[26:33], v[58:65], v[130:133], v214, v214 op_sel_hi:[0,0,0]
	s_setprio 0
	s_barrier
	s_add_i32 s42, s44, s48
	v_lshl_add_u64 v[218:219], v[218:219], 0, s[18:19]
	s_mov_b32 m0, s42
	s_nop 0
	global_load_lds_dwordx4 v[218:219], off
	v_lshl_add_u64 v[218:219], v[220:221], 0, s[18:19]
	s_add_i32 m0, s42, 0x2000
	s_add_i32 s42, s45, s48
	global_load_lds_dwordx4 v[218:219], off
	v_lshl_add_u64 v[218:219], v[222:223], 0, s[18:19]
	s_mov_b32 m0, s42
	s_nop 0
	global_load_lds_dwordx4 v[218:219], off
	v_lshl_add_u64 v[218:219], v[224:225], 0, s[18:19]
	s_add_i32 m0, s42, 0x2000
	s_nop 0
	global_load_lds_dwordx4 v[218:219], off
	v_lshl_add_u64 v[218:219], v[226:227], 0, s[18:19]
	s_mov_b32 m0, s59
	s_nop 0
	global_load_lds_dwordx4 v[218:219], off
	v_lshl_add_u64 v[218:219], v[228:229], 0, s[18:19]
	s_mov_b32 m0, s60
	s_nop 0
	global_load_lds_dwordx4 v[218:219], off
	ds_read_b128 v[34:37], v213 offset:49152
	ds_read_b128 v[38:41], v213 offset:50176
	ds_read_b128 v[42:45], v213 offset:51200
	ds_read_b128 v[46:49], v213 offset:52224
	ds_read_b128 v[50:53], v213 offset:53248
	ds_read_b128 v[54:57], v213 offset:54272
	ds_read_b128 v[58:61], v213 offset:55296
	ds_read_b128 v[62:65], v213 offset:56320
	s_waitcnt vmcnt(8)
	s_waitcnt lgkmcnt(0)
	s_barrier
	s_setprio 1
	s_waitcnt lgkmcnt(0)
	v_mfma_scale_f32_16x16x128_f8f6f4 v[126:129], v[2:9], v[34:41], v[126:129], v214, v214 op_sel_hi:[0,0,0]
	v_mfma_scale_f32_16x16x128_f8f6f4 v[122:125], v[10:17], v[34:41], v[122:125], v214, v214 op_sel_hi:[0,0,0]
	v_mfma_scale_f32_16x16x128_f8f6f4 v[110:113], v[2:9], v[42:49], v[110:113], v214, v214 op_sel_hi:[0,0,0]
	v_mfma_scale_f32_16x16x128_f8f6f4 v[106:109], v[10:17], v[42:49], v[106:109], v214, v214 op_sel_hi:[0,0,0]
	v_mfma_scale_f32_16x16x128_f8f6f4 v[94:97], v[2:9], v[50:57], v[94:97], v214, v214 op_sel_hi:[0,0,0]
	v_mfma_scale_f32_16x16x128_f8f6f4 v[90:93], v[10:17], v[50:57], v[90:93], v214, v214 op_sel_hi:[0,0,0]
	v_mfma_scale_f32_16x16x128_f8f6f4 v[78:81], v[2:9], v[58:65], v[78:81], v214, v214 op_sel_hi:[0,0,0]
	v_mfma_scale_f32_16x16x128_f8f6f4 v[74:77], v[10:17], v[58:65], v[74:77], v214, v214 op_sel_hi:[0,0,0]
	s_setprio 0
	s_setprio 1
	v_mfma_scale_f32_16x16x128_f8f6f4 v[118:121], v[18:25], v[34:41], v[118:121], v214, v214 op_sel_hi:[0,0,0]
	v_mfma_scale_f32_16x16x128_f8f6f4 v[114:117], v[26:33], v[34:41], v[114:117], v214, v214 op_sel_hi:[0,0,0]
	v_mfma_scale_f32_16x16x128_f8f6f4 v[102:105], v[18:25], v[42:49], v[102:105], v214, v214 op_sel_hi:[0,0,0]
	v_mfma_scale_f32_16x16x128_f8f6f4 v[98:101], v[26:33], v[42:49], v[98:101], v214, v214 op_sel_hi:[0,0,0]
	v_mfma_scale_f32_16x16x128_f8f6f4 v[86:89], v[18:25], v[50:57], v[86:89], v214, v214 op_sel_hi:[0,0,0]
	v_mfma_scale_f32_16x16x128_f8f6f4 v[82:85], v[26:33], v[50:57], v[82:85], v214, v214 op_sel_hi:[0,0,0]
	v_mfma_scale_f32_16x16x128_f8f6f4 v[70:73], v[18:25], v[58:65], v[70:73], v214, v214 op_sel_hi:[0,0,0]
	v_mfma_scale_f32_16x16x128_f8f6f4 v[66:69], v[26:33], v[58:65], v[66:69], v214, v214 op_sel_hi:[0,0,0]
	s_setprio 0
	s_barrier
	s_add_u32 s40, s40, 0x100
	s_addc_u32 s41, s41, 0
	s_add_u32 s68, s68, 0x100
	s_addc_u32 s69, s69, 0
	s_cmp_ge_i32 s70, s5
	s_cbranch_scc1 .LBB0_237

.LBB0_533:
	s_add_i32 s70, s70, 2
	s_waitcnt vmcnt(8)
	s_add_u32 s44, s40, 0x80
	s_waitcnt lgkmcnt(0)
	s_addc_u32 s45, s41, 0
	s_and_b64 s[42:43], s[42:43], exec
	v_mov_b32_e32 v201, v199
	v_mov_b32_e32 v205, v199
	s_cselect_b32 s43, s66, s45
	s_cselect_b32 s42, s67, s44
	s_cselect_b32 s45, s73, s69
	s_cselect_b32 s44, s74, s68
	s_barrier
	s_setprio 1
	s_waitcnt lgkmcnt(0)
	v_mfma_scale_f32_16x16x128_f8f6f4 v[190:193], v[18:25], v[58:65], v[190:193], v214, v214 op_sel_hi:[0,0,0]
	v_mfma_scale_f32_16x16x128_f8f6f4 v[186:189], v[26:33], v[58:65], v[186:189], v214, v214 op_sel_hi:[0,0,0]
	v_mfma_scale_f32_16x16x128_f8f6f4 v[182:185], v[18:25], v[50:57], v[182:185], v214, v214 op_sel_hi:[0,0,0]
	v_mfma_scale_f32_16x16x128_f8f6f4 v[178:181], v[26:33], v[50:57], v[178:181], v214, v214 op_sel_hi:[0,0,0]
	v_mfma_scale_f32_16x16x128_f8f6f4 v[170:173], v[18:25], v[42:49], v[170:173], v214, v214 op_sel_hi:[0,0,0]
	v_mfma_scale_f32_16x16x128_f8f6f4 v[162:165], v[26:33], v[42:49], v[162:165], v214, v214 op_sel_hi:[0,0,0]
	v_mfma_scale_f32_16x16x128_f8f6f4 v[154:157], v[18:25], v[34:41], v[154:157], v214, v214 op_sel_hi:[0,0,0]
	v_mfma_scale_f32_16x16x128_f8f6f4 v[146:149], v[26:33], v[34:41], v[146:149], v214, v214 op_sel_hi:[0,0,0]
	s_setprio 0
	s_setprio 1
	v_mfma_scale_f32_16x16x128_f8f6f4 v[174:177], v[2:9], v[58:65], v[174:177], v214, v214 op_sel_hi:[0,0,0]
	v_mfma_scale_f32_16x16x128_f8f6f4 v[166:169], v[10:17], v[58:65], v[166:169], v214, v214 op_sel_hi:[0,0,0]
	v_mfma_scale_f32_16x16x128_f8f6f4 v[158:161], v[2:9], v[50:57], v[158:161], v214, v214 op_sel_hi:[0,0,0]
	v_mfma_scale_f32_16x16x128_f8f6f4 v[150:153], v[10:17], v[50:57], v[150:153], v214, v214 op_sel_hi:[0,0,0]
	v_mfma_scale_f32_16x16x128_f8f6f4 v[142:145], v[2:9], v[42:49], v[142:145], v214, v214 op_sel_hi:[0,0,0]
	v_mfma_scale_f32_16x16x128_f8f6f4 v[138:141], v[10:17], v[42:49], v[138:141], v214, v214 op_sel_hi:[0,0,0]
	v_mfma_scale_f32_16x16x128_f8f6f4 v[134:137], v[2:9], v[34:41], v[134:137], v214, v214 op_sel_hi:[0,0,0]
	v_mfma_scale_f32_16x16x128_f8f6f4 v[130:133], v[10:17], v[34:41], v[130:133], v214, v214 op_sel_hi:[0,0,0]
	s_setprio 0
	s_barrier
	s_mov_b32 m0, s48
	v_lshl_add_u64 v[216:217], s[44:45], 0, v[194:195]
	v_lshl_add_u64 v[218:219], s[44:45], 0, v[196:197]
	s_add_u32 s44, s44, s10
	global_load_lds_dwordx4 v[216:217], off
	s_mov_b32 m0, s49
	s_addc_u32 s45, s45, s11
	global_load_lds_dwordx4 v[218:219], off
	v_lshl_add_u64 v[220:221], s[44:45], 0, v[194:195]
	s_mov_b32 m0, s50
	v_lshl_add_u64 v[222:223], s[44:45], 0, v[196:197]
	global_load_lds_dwordx4 v[220:221], off
	s_mov_b32 m0, s51
	v_mov_b32_e32 v203, v199
	global_load_lds_dwordx4 v[222:223], off
	s_mov_b32 m0, s47
	v_lshl_add_u64 v[224:225], s[42:43], 0, v[198:199]
	global_load_lds_dwordx4 v198, s[42:43]
	s_mov_b32 m0, s52
	v_lshl_add_u64 v[226:227], s[42:43], 0, v[202:203]
	global_load_lds_dwordx4 v202, s[42:43]
	ds_read_b128 v[34:37], v213 offset:16384
	ds_read_b128 v[38:41], v213 offset:17408
	ds_read_b128 v[42:45], v213 offset:18432
	ds_read_b128 v[46:49], v213 offset:19456
	ds_read_b128 v[50:53], v213 offset:20480
	ds_read_b128 v[54:57], v213 offset:21504
	ds_read_b128 v[58:61], v213 offset:22528
	ds_read_b128 v[62:65], v213 offset:23552
	s_waitcnt vmcnt(8)
	s_waitcnt lgkmcnt(0)
	s_barrier
	s_setprio 1
	s_waitcnt lgkmcnt(0)
	v_mfma_scale_f32_16x16x128_f8f6f4 v[126:129], v[18:25], v[34:41], v[126:129], v214, v214 op_sel_hi:[0,0,0]
	v_mfma_scale_f32_16x16x128_f8f6f4 v[122:125], v[26:33], v[34:41], v[122:125], v214, v214 op_sel_hi:[0,0,0]
	v_mfma_scale_f32_16x16x128_f8f6f4 v[118:121], v[18:25], v[42:49], v[118:121], v214, v214 op_sel_hi:[0,0,0]
	v_mfma_scale_f32_16x16x128_f8f6f4 v[114:117], v[26:33], v[42:49], v[114:117], v214, v214 op_sel_hi:[0,0,0]
	v_mfma_scale_f32_16x16x128_f8f6f4 v[106:109], v[18:25], v[50:57], v[106:109], v214, v214 op_sel_hi:[0,0,0]
	v_mfma_scale_f32_16x16x128_f8f6f4 v[98:101], v[26:33], v[50:57], v[98:101], v214, v214 op_sel_hi:[0,0,0]
	v_mfma_scale_f32_16x16x128_f8f6f4 v[90:93], v[18:25], v[58:65], v[90:93], v214, v214 op_sel_hi:[0,0,0]
	v_mfma_scale_f32_16x16x128_f8f6f4 v[82:85], v[26:33], v[58:65], v[82:85], v214, v214 op_sel_hi:[0,0,0]
	s_setprio 0
	s_setprio 1
	v_mfma_scale_f32_16x16x128_f8f6f4 v[110:113], v[2:9], v[34:41], v[110:113], v214, v214 op_sel_hi:[0,0,0]
	v_mfma_scale_f32_16x16x128_f8f6f4 v[102:105], v[10:17], v[34:41], v[102:105], v214, v214 op_sel_hi:[0,0,0]
	v_mfma_scale_f32_16x16x128_f8f6f4 v[94:97], v[2:9], v[42:49], v[94:97], v214, v214 op_sel_hi:[0,0,0]
	v_mfma_scale_f32_16x16x128_f8f6f4 v[86:89], v[10:17], v[42:49], v[86:89], v214, v214 op_sel_hi:[0,0,0]
	v_mfma_scale_f32_16x16x128_f8f6f4 v[78:81], v[2:9], v[50:57], v[78:81], v214, v214 op_sel_hi:[0,0,0]
	v_mfma_scale_f32_16x16x128_f8f6f4 v[74:77], v[10:17], v[50:57], v[74:77], v214, v214 op_sel_hi:[0,0,0]
	v_mfma_scale_f32_16x16x128_f8f6f4 v[70:73], v[2:9], v[58:65], v[70:73], v214, v214 op_sel_hi:[0,0,0]
	v_mfma_scale_f32_16x16x128_f8f6f4 v[66:69], v[10:17], v[58:65], v[66:69], v214, v214 op_sel_hi:[0,0,0]
	s_setprio 0
	s_barrier
	s_add_i32 s44, 0, 0x18000
	s_add_i32 s45, 0, 0x1c000
	v_add_u32_e32 v14, s44, v209
	v_add_u32_e32 v30, s45, v209
	s_mov_b32 m0, s53
	v_lshl_add_u64 v[228:229], s[42:43], 0, v[200:201]
	global_load_lds_dwordx4 v[228:229], off
	v_lshl_add_u64 v[228:229], s[42:43], 0, v[204:205]
	s_mov_b32 m0, s54
	s_nop 0
	global_load_lds_dwordx4 v[228:229], off
	ds_read_b128 v[2:5], v14
	ds_read_b128 v[6:9], v14 offset:1024
	ds_read_b128 v[10:13], v14 offset:2048
	ds_read_b128 v[14:17], v14 offset:3072
	ds_read_b128 v[18:21], v30
	ds_read_b128 v[22:25], v30 offset:1024
	ds_read_b128 v[26:29], v30 offset:2048
	ds_read_b128 v[30:33], v30 offset:3072
	ds_read_b128 v[34:37], v213 offset:32768
	ds_read_b128 v[38:41], v213 offset:33792
	ds_read_b128 v[42:45], v213 offset:34816
	ds_read_b128 v[46:49], v213 offset:35840
	ds_read_b128 v[50:53], v213 offset:36864
	ds_read_b128 v[54:57], v213 offset:37888
	ds_read_b128 v[58:61], v213 offset:38912
	ds_read_b128 v[62:65], v213 offset:39936
	s_waitcnt vmcnt(8)
	s_waitcnt lgkmcnt(0)
	s_barrier
	s_setprio 1
	s_waitcnt lgkmcnt(0)
	v_mfma_scale_f32_16x16x128_f8f6f4 v[190:193], v[2:9], v[34:41], v[190:193], v214, v214 op_sel_hi:[0,0,0]
	v_mfma_scale_f32_16x16x128_f8f6f4 v[186:189], v[10:17], v[34:41], v[186:189], v214, v214 op_sel_hi:[0,0,0]
	v_mfma_scale_f32_16x16x128_f8f6f4 v[182:185], v[2:9], v[42:49], v[182:185], v214, v214 op_sel_hi:[0,0,0]
	v_mfma_scale_f32_16x16x128_f8f6f4 v[178:181], v[10:17], v[42:49], v[178:181], v214, v214 op_sel_hi:[0,0,0]
	v_mfma_scale_f32_16x16x128_f8f6f4 v[170:173], v[2:9], v[50:57], v[170:173], v214, v214 op_sel_hi:[0,0,0]
	v_mfma_scale_f32_16x16x128_f8f6f4 v[162:165], v[10:17], v[50:57], v[162:165], v214, v214 op_sel_hi:[0,0,0]
	v_mfma_scale_f32_16x16x128_f8f6f4 v[154:157], v[2:9], v[58:65], v[154:157], v214, v214 op_sel_hi:[0,0,0]
	v_mfma_scale_f32_16x16x128_f8f6f4 v[146:149], v[10:17], v[58:65], v[146:149], v214, v214 op_sel_hi:[0,0,0]
	s_setprio 0
	s_setprio 1
	v_mfma_scale_f32_16x16x128_f8f6f4 v[174:177], v[18:25], v[34:41], v[174:177], v214, v214 op_sel_hi:[0,0,0]
	v_mfma_scale_f32_16x16x128_f8f6f4 v[166:169], v[26:33], v[34:41], v[166:169], v214, v214 op_sel_hi:[0,0,0]
	v_mfma_scale_f32_16x16x128_f8f6f4 v[158:161], v[18:25], v[42:49], v[158:161], v214, v214 op_sel_hi:[0,0,0]
	v_mfma_scale_f32_16x16x128_f8f6f4 v[150:153], v[26:33], v[42:49], v[150:153], v214, v214 op_sel_hi:[0,0,0]
	v_mfma_scale_f32_16x16x128_f8f6f4 v[142:145], v[18:25], v[50:57], v[142:145], v214, v214 op_sel_hi:[0,0,0]
	v_mfma_scale_f32_16x16x128_f8f6f4 v[138:141], v[26:33], v[50:57], v[138:141], v214, v214 op_sel_hi:[0,0,0]
	v_mfma_scale_f32_16x16x128_f8f6f4 v[134:137], v[18:25], v[58:65], v[134:137], v214, v214 op_sel_hi:[0,0,0]
	v_mfma_scale_f32_16x16x128_f8f6f4 v[130:133], v[26:33], v[58:65], v[130:133], v214, v214 op_sel_hi:[0,0,0]
	s_setprio 0
	s_barrier
	s_add_i32 s42, s44, s23
	v_lshl_add_u64 v[216:217], v[216:217], 0, s[16:17]
	s_mov_b32 m0, s42
	s_nop 0
	global_load_lds_dwordx4 v[216:217], off
	v_lshl_add_u64 v[216:217], v[218:219], 0, s[16:17]
	s_add_i32 m0, s42, 0x2000
	s_add_i32 s42, s45, s23
	global_load_lds_dwordx4 v[216:217], off
	v_lshl_add_u64 v[216:217], v[220:221], 0, s[16:17]
	s_mov_b32 m0, s42
	s_nop 0
	global_load_lds_dwordx4 v[216:217], off
	v_lshl_add_u64 v[216:217], v[222:223], 0, s[16:17]
	s_add_i32 m0, s42, 0x2000
	s_nop 0
	global_load_lds_dwordx4 v[216:217], off
	v_lshl_add_u64 v[216:217], v[224:225], 0, s[16:17]
	s_mov_b32 m0, s57
	s_nop 0
	global_load_lds_dwordx4 v[216:217], off
	v_lshl_add_u64 v[216:217], v[226:227], 0, s[16:17]
	s_mov_b32 m0, s58
	s_nop 0
	global_load_lds_dwordx4 v[216:217], off
	ds_read_b128 v[34:37], v213 offset:49152
	ds_read_b128 v[38:41], v213 offset:50176
	ds_read_b128 v[42:45], v213 offset:51200
	ds_read_b128 v[46:49], v213 offset:52224
	ds_read_b128 v[50:53], v213 offset:53248
	ds_read_b128 v[54:57], v213 offset:54272
	ds_read_b128 v[58:61], v213 offset:55296
	ds_read_b128 v[62:65], v213 offset:56320
	s_waitcnt vmcnt(8)
	s_waitcnt lgkmcnt(0)
	s_barrier
	s_setprio 1
	s_waitcnt lgkmcnt(0)
	v_mfma_scale_f32_16x16x128_f8f6f4 v[126:129], v[2:9], v[34:41], v[126:129], v214, v214 op_sel_hi:[0,0,0]
	v_mfma_scale_f32_16x16x128_f8f6f4 v[122:125], v[10:17], v[34:41], v[122:125], v214, v214 op_sel_hi:[0,0,0]
	v_mfma_scale_f32_16x16x128_f8f6f4 v[118:121], v[2:9], v[42:49], v[118:121], v214, v214 op_sel_hi:[0,0,0]
	v_mfma_scale_f32_16x16x128_f8f6f4 v[114:117], v[10:17], v[42:49], v[114:117], v214, v214 op_sel_hi:[0,0,0]
	v_mfma_scale_f32_16x16x128_f8f6f4 v[106:109], v[2:9], v[50:57], v[106:109], v214, v214 op_sel_hi:[0,0,0]
	v_mfma_scale_f32_16x16x128_f8f6f4 v[98:101], v[10:17], v[50:57], v[98:101], v214, v214 op_sel_hi:[0,0,0]
	v_mfma_scale_f32_16x16x128_f8f6f4 v[90:93], v[2:9], v[58:65], v[90:93], v214, v214 op_sel_hi:[0,0,0]
	v_mfma_scale_f32_16x16x128_f8f6f4 v[82:85], v[10:17], v[58:65], v[82:85], v214, v214 op_sel_hi:[0,0,0]
	s_setprio 0
	s_setprio 1
	v_mfma_scale_f32_16x16x128_f8f6f4 v[110:113], v[18:25], v[34:41], v[110:113], v214, v214 op_sel_hi:[0,0,0]
	v_mfma_scale_f32_16x16x128_f8f6f4 v[102:105], v[26:33], v[34:41], v[102:105], v214, v214 op_sel_hi:[0,0,0]
	v_mfma_scale_f32_16x16x128_f8f6f4 v[94:97], v[18:25], v[42:49], v[94:97], v214, v214 op_sel_hi:[0,0,0]
	v_mfma_scale_f32_16x16x128_f8f6f4 v[86:89], v[26:33], v[42:49], v[86:89], v214, v214 op_sel_hi:[0,0,0]
	v_mfma_scale_f32_16x16x128_f8f6f4 v[78:81], v[18:25], v[50:57], v[78:81], v214, v214 op_sel_hi:[0,0,0]
	v_mfma_scale_f32_16x16x128_f8f6f4 v[74:77], v[26:33], v[50:57], v[74:77], v214, v214 op_sel_hi:[0,0,0]
	v_mfma_scale_f32_16x16x128_f8f6f4 v[70:73], v[18:25], v[58:65], v[70:73], v214, v214 op_sel_hi:[0,0,0]
	v_mfma_scale_f32_16x16x128_f8f6f4 v[66:69], v[26:33], v[58:65], v[66:69], v214, v214 op_sel_hi:[0,0,0]
	s_setprio 0
	s_barrier
	s_add_u32 s40, s40, 0x100
	s_addc_u32 s41, s41, 0
	s_add_u32 s68, s68, 0x100
	s_addc_u32 s69, s69, 0
	s_cmp_ge_i32 s70, s7
	s_cbranch_scc1 .LBB0_537

.LBB0_1135:
	s_add_i32 s83, s83, 2
	s_waitcnt vmcnt(8)
	s_add_u32 s46, s42, 0x80
	s_waitcnt lgkmcnt(0)
	s_addc_u32 s47, s43, 0
	s_and_b64 s[4:5], s[44:45], exec
	v_mov_b32_e32 v219, v195
	s_cselect_b32 s5, s35, s47
	s_cselect_b32 s4, s34, s46
	s_cselect_b32 s45, s31, s82
	s_cselect_b32 s44, s30, s81
	s_barrier
	s_setprio 1
	s_waitcnt lgkmcnt(0)
	v_mfma_scale_f32_16x16x128_f8f6f4 v[186:189], v[18:25], v[58:65], v[186:189], v228, v228 op_sel_hi:[0,0,0]
	v_mfma_scale_f32_16x16x128_f8f6f4 v[182:185], v[26:33], v[58:65], v[182:185], v228, v228 op_sel_hi:[0,0,0]
	v_mfma_scale_f32_16x16x128_f8f6f4 v[174:177], v[18:25], v[50:57], v[174:177], v228, v228 op_sel_hi:[0,0,0]
	v_mfma_scale_f32_16x16x128_f8f6f4 v[166:169], v[26:33], v[50:57], v[166:169], v228, v228 op_sel_hi:[0,0,0]
	v_mfma_scale_f32_16x16x128_f8f6f4 v[158:161], v[18:25], v[42:49], v[158:161], v228, v228 op_sel_hi:[0,0,0]
	v_mfma_scale_f32_16x16x128_f8f6f4 v[150:153], v[26:33], v[42:49], v[150:153], v228, v228 op_sel_hi:[0,0,0]
	v_mfma_scale_f32_16x16x128_f8f6f4 v[142:145], v[18:25], v[34:41], v[142:145], v228, v228 op_sel_hi:[0,0,0]
	v_mfma_scale_f32_16x16x128_f8f6f4 v[134:137], v[26:33], v[34:41], v[134:137], v228, v228 op_sel_hi:[0,0,0]
	s_setprio 0
	s_setprio 1
	v_mfma_scale_f32_16x16x128_f8f6f4 v[190:193], v[2:9], v[58:65], v[190:193], v228, v228 op_sel_hi:[0,0,0]
	v_mfma_scale_f32_16x16x128_f8f6f4 v[178:181], v[10:17], v[58:65], v[178:181], v228, v228 op_sel_hi:[0,0,0]
	v_mfma_scale_f32_16x16x128_f8f6f4 v[170:173], v[2:9], v[50:57], v[170:173], v228, v228 op_sel_hi:[0,0,0]
	v_mfma_scale_f32_16x16x128_f8f6f4 v[162:165], v[10:17], v[50:57], v[162:165], v228, v228 op_sel_hi:[0,0,0]
	v_mfma_scale_f32_16x16x128_f8f6f4 v[154:157], v[2:9], v[42:49], v[154:157], v228, v228 op_sel_hi:[0,0,0]
	v_mfma_scale_f32_16x16x128_f8f6f4 v[146:149], v[10:17], v[42:49], v[146:149], v228, v228 op_sel_hi:[0,0,0]
	v_mfma_scale_f32_16x16x128_f8f6f4 v[138:141], v[2:9], v[34:41], v[138:141], v228, v228 op_sel_hi:[0,0,0]
	v_mfma_scale_f32_16x16x128_f8f6f4 v[130:133], v[10:17], v[34:41], v[130:133], v228, v228 op_sel_hi:[0,0,0]
	s_setprio 0
	s_barrier
	s_mov_b32 m0, s58
	v_lshl_add_u64 v[232:233], s[44:45], 0, v[196:197]
	v_lshl_add_u64 v[234:235], s[44:45], 0, v[198:199]
	s_add_u32 s44, s44, s16
	global_load_lds_dwordx4 v[232:233], off
	s_mov_b32 m0, s59
	s_addc_u32 s45, s45, s17
	global_load_lds_dwordx4 v[234:235], off
	v_lshl_add_u64 v[236:237], s[44:45], 0, v[196:197]
	s_mov_b32 m0, s60
	v_lshl_add_u64 v[238:239], s[44:45], 0, v[198:199]
	global_load_lds_dwordx4 v[236:237], off
	s_mov_b32 m0, s61
	v_mov_b32_e32 v203, v195
	global_load_lds_dwordx4 v[238:239], off
	s_mov_b32 m0, s57
	v_mov_b32_e32 v201, v195
	global_load_lds_dwordx4 v202, s[4:5]
	s_mov_b32 m0, s62
	v_lshl_add_u64 v[240:241], s[4:5], 0, v[202:203]
	global_load_lds_dwordx4 v200, s[4:5]
	ds_read_b128 v[34:37], v227 offset:16384
	ds_read_b128 v[38:41], v227 offset:17408
	ds_read_b128 v[42:45], v227 offset:18432
	ds_read_b128 v[46:49], v227 offset:19456
	ds_read_b128 v[50:53], v227 offset:20480
	ds_read_b128 v[54:57], v227 offset:21504
	ds_read_b128 v[58:61], v227 offset:22528
	ds_read_b128 v[62:65], v227 offset:23552
	s_waitcnt vmcnt(8)
	s_waitcnt lgkmcnt(0)
	v_lshl_add_u64 v[242:243], s[4:5], 0, v[200:201]
	s_barrier
	s_setprio 1
	s_waitcnt lgkmcnt(0)
	v_mfma_scale_f32_16x16x128_f8f6f4 v[126:129], v[18:25], v[34:41], v[126:129], v228, v228 op_sel_hi:[0,0,0]
	v_mfma_scale_f32_16x16x128_f8f6f4 v[118:121], v[26:33], v[34:41], v[118:121], v228, v228 op_sel_hi:[0,0,0]
	v_mfma_scale_f32_16x16x128_f8f6f4 v[110:113], v[18:25], v[42:49], v[110:113], v228, v228 op_sel_hi:[0,0,0]
	v_mfma_scale_f32_16x16x128_f8f6f4 v[102:105], v[26:33], v[42:49], v[102:105], v228, v228 op_sel_hi:[0,0,0]
	v_mfma_scale_f32_16x16x128_f8f6f4 v[94:97], v[18:25], v[50:57], v[94:97], v228, v228 op_sel_hi:[0,0,0]
	v_mfma_scale_f32_16x16x128_f8f6f4 v[86:89], v[26:33], v[50:57], v[86:89], v228, v228 op_sel_hi:[0,0,0]
	v_mfma_scale_f32_16x16x128_f8f6f4 v[78:81], v[18:25], v[58:65], v[78:81], v228, v228 op_sel_hi:[0,0,0]
	v_mfma_scale_f32_16x16x128_f8f6f4 v[70:73], v[26:33], v[58:65], v[70:73], v228, v228 op_sel_hi:[0,0,0]
	s_setprio 0
	s_setprio 1
	v_mfma_scale_f32_16x16x128_f8f6f4 v[122:125], v[2:9], v[34:41], v[122:125], v228, v228 op_sel_hi:[0,0,0]
	v_mfma_scale_f32_16x16x128_f8f6f4 v[114:117], v[10:17], v[34:41], v[114:117], v228, v228 op_sel_hi:[0,0,0]
	v_mfma_scale_f32_16x16x128_f8f6f4 v[106:109], v[2:9], v[42:49], v[106:109], v228, v228 op_sel_hi:[0,0,0]
	v_mfma_scale_f32_16x16x128_f8f6f4 v[98:101], v[10:17], v[42:49], v[98:101], v228, v228 op_sel_hi:[0,0,0]
	v_mfma_scale_f32_16x16x128_f8f6f4 v[90:93], v[2:9], v[50:57], v[90:93], v228, v228 op_sel_hi:[0,0,0]
	v_mfma_scale_f32_16x16x128_f8f6f4 v[82:85], v[10:17], v[50:57], v[82:85], v228, v228 op_sel_hi:[0,0,0]
	v_mfma_scale_f32_16x16x128_f8f6f4 v[74:77], v[2:9], v[58:65], v[74:77], v228, v228 op_sel_hi:[0,0,0]
	v_mfma_scale_f32_16x16x128_f8f6f4 v[66:69], v[10:17], v[58:65], v[66:69], v228, v228 op_sel_hi:[0,0,0]
	s_setprio 0
	s_barrier
	s_add_i32 s44, 0, 0x18000
	s_add_i32 s45, 0, 0x1c000
	v_add_u32_e32 v14, s44, v222
	v_add_u32_e32 v30, s45, v222
	s_mov_b32 m0, s63
	v_lshl_add_u64 v[244:245], s[4:5], 0, v[194:195]
	global_load_lds_dwordx4 v[244:245], off
	v_lshl_add_u64 v[244:245], s[4:5], 0, v[218:219]
	s_mov_b32 m0, s64
	s_nop 0
	global_load_lds_dwordx4 v[244:245], off
	ds_read_b128 v[2:5], v14
	ds_read_b128 v[6:9], v14 offset:1024
	ds_read_b128 v[10:13], v14 offset:2048
	ds_read_b128 v[14:17], v14 offset:3072
	ds_read_b128 v[18:21], v30
	ds_read_b128 v[22:25], v30 offset:1024
	ds_read_b128 v[26:29], v30 offset:2048
	ds_read_b128 v[30:33], v30 offset:3072
	ds_read_b128 v[34:37], v227 offset:32768
	ds_read_b128 v[38:41], v227 offset:33792
	ds_read_b128 v[42:45], v227 offset:34816
	ds_read_b128 v[46:49], v227 offset:35840
	ds_read_b128 v[50:53], v227 offset:36864
	ds_read_b128 v[54:57], v227 offset:37888
	ds_read_b128 v[58:61], v227 offset:38912
	ds_read_b128 v[62:65], v227 offset:39936
	s_waitcnt vmcnt(8)
	s_waitcnt lgkmcnt(0)
	s_barrier
	s_setprio 1
	s_waitcnt lgkmcnt(0)
	v_mfma_scale_f32_16x16x128_f8f6f4 v[186:189], v[2:9], v[34:41], v[186:189], v228, v228 op_sel_hi:[0,0,0]
	v_mfma_scale_f32_16x16x128_f8f6f4 v[182:185], v[10:17], v[34:41], v[182:185], v228, v228 op_sel_hi:[0,0,0]
	v_mfma_scale_f32_16x16x128_f8f6f4 v[174:177], v[2:9], v[42:49], v[174:177], v228, v228 op_sel_hi:[0,0,0]
	v_mfma_scale_f32_16x16x128_f8f6f4 v[166:169], v[10:17], v[42:49], v[166:169], v228, v228 op_sel_hi:[0,0,0]
	v_mfma_scale_f32_16x16x128_f8f6f4 v[158:161], v[2:9], v[50:57], v[158:161], v228, v228 op_sel_hi:[0,0,0]
	v_mfma_scale_f32_16x16x128_f8f6f4 v[150:153], v[10:17], v[50:57], v[150:153], v228, v228 op_sel_hi:[0,0,0]
	v_mfma_scale_f32_16x16x128_f8f6f4 v[142:145], v[2:9], v[58:65], v[142:145], v228, v228 op_sel_hi:[0,0,0]
	v_mfma_scale_f32_16x16x128_f8f6f4 v[134:137], v[10:17], v[58:65], v[134:137], v228, v228 op_sel_hi:[0,0,0]
	s_setprio 0
	s_setprio 1
	v_mfma_scale_f32_16x16x128_f8f6f4 v[190:193], v[18:25], v[34:41], v[190:193], v228, v228 op_sel_hi:[0,0,0]
	v_mfma_scale_f32_16x16x128_f8f6f4 v[178:181], v[26:33], v[34:41], v[178:181], v228, v228 op_sel_hi:[0,0,0]
	v_mfma_scale_f32_16x16x128_f8f6f4 v[170:173], v[18:25], v[42:49], v[170:173], v228, v228 op_sel_hi:[0,0,0]
	v_mfma_scale_f32_16x16x128_f8f6f4 v[162:165], v[26:33], v[42:49], v[162:165], v228, v228 op_sel_hi:[0,0,0]
	v_mfma_scale_f32_16x16x128_f8f6f4 v[154:157], v[18:25], v[50:57], v[154:157], v228, v228 op_sel_hi:[0,0,0]
	v_mfma_scale_f32_16x16x128_f8f6f4 v[146:149], v[26:33], v[50:57], v[146:149], v228, v228 op_sel_hi:[0,0,0]
	v_mfma_scale_f32_16x16x128_f8f6f4 v[138:141], v[18:25], v[58:65], v[138:141], v228, v228 op_sel_hi:[0,0,0]
	v_mfma_scale_f32_16x16x128_f8f6f4 v[130:133], v[26:33], v[58:65], v[130:133], v228, v228 op_sel_hi:[0,0,0]
	s_setprio 0
	s_barrier
	s_add_i32 s4, s44, s56
	v_lshl_add_u64 v[232:233], v[232:233], 0, s[20:21]
	s_mov_b32 m0, s4
	s_nop 0
	global_load_lds_dwordx4 v[232:233], off
	v_lshl_add_u64 v[232:233], v[234:235], 0, s[20:21]
	s_add_i32 m0, s4, 0x2000
	s_add_i32 s4, s45, s56
	global_load_lds_dwordx4 v[232:233], off
	v_lshl_add_u64 v[232:233], v[236:237], 0, s[20:21]
	s_mov_b32 m0, s4
	s_nop 0
	global_load_lds_dwordx4 v[232:233], off
	v_lshl_add_u64 v[232:233], v[238:239], 0, s[20:21]
	s_add_i32 m0, s4, 0x2000
	s_nop 0
	global_load_lds_dwordx4 v[232:233], off
	v_lshl_add_u64 v[232:233], v[240:241], 0, s[20:21]
	s_mov_b32 m0, s66
	s_nop 0
	global_load_lds_dwordx4 v[232:233], off
	v_lshl_add_u64 v[232:233], v[242:243], 0, s[20:21]
	s_mov_b32 m0, s67
	s_nop 0
	global_load_lds_dwordx4 v[232:233], off
	ds_read_b128 v[34:37], v227 offset:49152
	ds_read_b128 v[38:41], v227 offset:50176
	ds_read_b128 v[42:45], v227 offset:51200
	ds_read_b128 v[46:49], v227 offset:52224
	ds_read_b128 v[50:53], v227 offset:53248
	ds_read_b128 v[54:57], v227 offset:54272
	ds_read_b128 v[58:61], v227 offset:55296
	ds_read_b128 v[62:65], v227 offset:56320
	s_waitcnt vmcnt(8)
	s_waitcnt lgkmcnt(0)
	s_barrier
	s_setprio 1
	s_waitcnt lgkmcnt(0)
	v_mfma_scale_f32_16x16x128_f8f6f4 v[126:129], v[2:9], v[34:41], v[126:129], v228, v228 op_sel_hi:[0,0,0]
	v_mfma_scale_f32_16x16x128_f8f6f4 v[118:121], v[10:17], v[34:41], v[118:121], v228, v228 op_sel_hi:[0,0,0]
	v_mfma_scale_f32_16x16x128_f8f6f4 v[110:113], v[2:9], v[42:49], v[110:113], v228, v228 op_sel_hi:[0,0,0]
	v_mfma_scale_f32_16x16x128_f8f6f4 v[102:105], v[10:17], v[42:49], v[102:105], v228, v228 op_sel_hi:[0,0,0]
	v_mfma_scale_f32_16x16x128_f8f6f4 v[94:97], v[2:9], v[50:57], v[94:97], v228, v228 op_sel_hi:[0,0,0]
	v_mfma_scale_f32_16x16x128_f8f6f4 v[86:89], v[10:17], v[50:57], v[86:89], v228, v228 op_sel_hi:[0,0,0]
	v_mfma_scale_f32_16x16x128_f8f6f4 v[78:81], v[2:9], v[58:65], v[78:81], v228, v228 op_sel_hi:[0,0,0]
	v_mfma_scale_f32_16x16x128_f8f6f4 v[70:73], v[10:17], v[58:65], v[70:73], v228, v228 op_sel_hi:[0,0,0]
	s_setprio 0
	s_setprio 1
	v_mfma_scale_f32_16x16x128_f8f6f4 v[122:125], v[18:25], v[34:41], v[122:125], v228, v228 op_sel_hi:[0,0,0]
	v_mfma_scale_f32_16x16x128_f8f6f4 v[114:117], v[26:33], v[34:41], v[114:117], v228, v228 op_sel_hi:[0,0,0]
	v_mfma_scale_f32_16x16x128_f8f6f4 v[106:109], v[18:25], v[42:49], v[106:109], v228, v228 op_sel_hi:[0,0,0]
	v_mfma_scale_f32_16x16x128_f8f6f4 v[98:101], v[26:33], v[42:49], v[98:101], v228, v228 op_sel_hi:[0,0,0]
	v_mfma_scale_f32_16x16x128_f8f6f4 v[90:93], v[18:25], v[50:57], v[90:93], v228, v228 op_sel_hi:[0,0,0]
	v_mfma_scale_f32_16x16x128_f8f6f4 v[82:85], v[26:33], v[50:57], v[82:85], v228, v228 op_sel_hi:[0,0,0]
	v_mfma_scale_f32_16x16x128_f8f6f4 v[74:77], v[18:25], v[58:65], v[74:77], v228, v228 op_sel_hi:[0,0,0]
	v_mfma_scale_f32_16x16x128_f8f6f4 v[66:69], v[26:33], v[58:65], v[66:69], v228, v228 op_sel_hi:[0,0,0]
	s_setprio 0
	s_barrier
	s_add_u32 s42, s42, 0x100
	s_addc_u32 s43, s43, 0
	s_add_u32 s81, s81, 0x100
	s_addc_u32 s82, s82, 0
	s_cmp_ge_i32 s83, s11
	s_cbranch_scc1 .LBB0_1154
